# baseline (speedup 1.0000x reference)
.Lp1_loop:
	s_waitcnt vmcnt(0)
	ds_write_b128 v88, v[146:149]
	ds_write_b128 v89, v[150:153]
	ds_write_b128 v88, v[154:157] offset:9216
	ds_write_b128 v89, v[158:161] offset:9216
	global_load_dwordx4 v[112:115], v128, s[24:25]
	global_load_dwordx4 v[116:119], v86, s[24:25]
	s_add_u32 s24, s24, 0x2000
	s_addc_u32 s25, s25, 0
	global_load_dwordx4 v[120:123], v128, s[24:25]
	global_load_dwordx4 v[124:127], v86, s[24:25]
	s_add_u32 s24, s24, 0x2000
	s_addc_u32 s25, s25, 0
	ds_read_b128 v[168:171], v167
	ds_read_b128 v[172:175], v167 offset:4608
	ds_read_b128 v[176:179], v167 offset:32
	ds_read_b128 v[180:183], v167 offset:4640
	ds_read_b128 v[184:187], v167 offset:64
	ds_read_b128 v[188:191], v167 offset:4672
	ds_read_b128 v[192:195], v167 offset:96
	ds_read_b128 v[196:199], v167 offset:4704
	v_exp_f32_e32 v34, v34
	v_mov_b32_e32 v200, 0
	v_exp_f32_e32 v35, v35
	v_mov_b32_e32 v201, 0
	v_exp_f32_e32 v36, v36
	v_mov_b32_e32 v202, 0
	s_waitcnt lgkmcnt(7)
	v_mfma_f32_32x32x16_f16 v[2:17], v[168:171], v[108:111], v[130:145]
	v_exp_f32_e32 v37, v37
	v_mov_b32_e32 v83, 0
	v_exp_f32_e32 v38, v38
	v_add_f32_e32 v200, v200, v34
	v_exp_f32_e32 v39, v39
	v_add_f32_e32 v201, v201, v35
	s_waitcnt lgkmcnt(6)
	v_mfma_f32_32x32x16_f16 v[18:33], v[172:175], v[108:111], v[130:145]
	v_exp_f32_e32 v40, v40
	v_add_f32_e32 v202, v202, v36
	v_exp_f32_e32 v41, v41
	v_add_f32_e32 v83, v83, v37
	v_exp_f32_e32 v42, v42
	v_add_f32_e32 v200, v200, v38
	s_waitcnt lgkmcnt(5)
	v_mfma_f32_32x32x16_f16 v[2:17], v[176:179], v[104:107], v[2:17]
	v_exp_f32_e32 v43, v43
	v_add_f32_e32 v201, v201, v39
	v_exp_f32_e32 v44, v44
	v_add_f32_e32 v202, v202, v40
	v_exp_f32_e32 v45, v45
	v_add_f32_e32 v83, v83, v41
	s_waitcnt lgkmcnt(4)
	v_mfma_f32_32x32x16_f16 v[18:33], v[180:183], v[104:107], v[18:33]
	v_exp_f32_e32 v46, v46
	v_add_f32_e32 v200, v200, v42
	v_exp_f32_e32 v47, v47
	v_add_f32_e32 v201, v201, v43
	v_exp_f32_e32 v48, v48
	v_add_f32_e32 v202, v202, v44
	s_waitcnt lgkmcnt(3)
	v_mfma_f32_32x32x16_f16 v[2:17], v[184:187], v[100:103], v[2:17]
	v_exp_f32_e32 v49, v49
	v_add_f32_e32 v83, v83, v45
	v_exp_f32_e32 v50, v50
	v_add_f32_e32 v200, v200, v46
	v_exp_f32_e32 v51, v51
	v_add_f32_e32 v201, v201, v47
	s_waitcnt lgkmcnt(2)
	v_mfma_f32_32x32x16_f16 v[18:33], v[188:191], v[100:103], v[18:33]
	v_exp_f32_e32 v52, v52
	v_add_f32_e32 v202, v202, v48
	v_exp_f32_e32 v53, v53
	v_add_f32_e32 v83, v83, v49
	v_exp_f32_e32 v54, v54
	v_add_f32_e32 v200, v200, v50
	s_waitcnt lgkmcnt(1)
	v_mfma_f32_32x32x16_f16 v[2:17], v[192:195], v[96:99], v[2:17]
	v_exp_f32_e32 v55, v55
	v_add_f32_e32 v201, v201, v51
	v_exp_f32_e32 v56, v56
	v_add_f32_e32 v202, v202, v52
	v_exp_f32_e32 v57, v57
	v_add_f32_e32 v83, v83, v53
	s_waitcnt lgkmcnt(0)
	v_mfma_f32_32x32x16_f16 v[18:33], v[196:199], v[96:99], v[18:33]
	ds_read_b128 v[204:207], v167 offset:9216
	ds_read_b128 v[208:211], v167 offset:13824
	ds_read_b128 v[212:215], v167 offset:9248
	ds_read_b128 v[216:219], v167 offset:13856
	ds_read_b128 v[220:223], v167 offset:9280
	ds_read_b128 v[224:227], v167 offset:13888
	ds_read_b128 v[228:231], v167 offset:9312
	ds_read_b128 v[232:235], v167 offset:13920
	v_exp_f32_e32 v58, v58
	v_add_f32_e32 v200, v200, v54
	v_exp_f32_e32 v59, v59
	v_add_f32_e32 v201, v201, v55
	v_exp_f32_e32 v60, v60
	v_add_f32_e32 v202, v202, v56
	v_exp_f32_e32 v61, v61
	v_add_f32_e32 v83, v83, v57
	v_exp_f32_e32 v62, v62
	v_add_f32_e32 v200, v200, v58
	v_exp_f32_e32 v63, v63
	v_add_f32_e32 v201, v201, v59
	v_exp_f32_e32 v64, v64
	v_add_f32_e32 v202, v202, v60
	v_exp_f32_e32 v65, v65
	v_add_f32_e32 v83, v83, v61
	v_add_f32_e32 v200, v200, v62
	v_add_f32_e32 v201, v201, v63
	v_add_f32_e32 v202, v202, v64
	v_add_f32_e32 v83, v83, v65
	v_add_f32_e32 v200, v200, v201
	v_add_f32_e32 v202, v202, v83
	v_add_f32_e32 v200, v200, v202
	v_add_f32_e32 v82, v82, v200
	v_max3_f32 v84, v2, v3, v4
	v_max3_f32 v85, v18, v19, v20
	v_max3_f32 v84, v84, v5, v6
	v_max3_f32 v85, v85, v21, v22
	v_max3_f32 v84, v84, v7, v8
	v_max3_f32 v85, v85, v23, v24
	v_max3_f32 v84, v84, v9, v10
	v_max3_f32 v85, v85, v25, v26
	v_max3_f32 v84, v84, v11, v12
	v_max3_f32 v85, v85, v27, v28
	v_max3_f32 v84, v84, v13, v14
	v_max3_f32 v85, v85, v29, v30
	v_max3_f32 v84, v84, v15, v16
	v_max3_f32 v85, v85, v31, v32
	v_max3_f32 v84, v84, v17, v33
	s_nop 0
	v_max_f32_e32 v84, v84, v85
	s_nop 0
	v_cmp_lt_f32_e32 vcc, s11, v84
	s_cbranch_vccnz .Lp1_rare_d0a
.Lp1_back_d0a:
	v_exp_f32_e32 v2, v2
	v_mov_b32_e32 v200, 0
	v_exp_f32_e32 v3, v3
	v_mov_b32_e32 v201, 0
	v_exp_f32_e32 v4, v4
	v_mov_b32_e32 v202, 0
	s_waitcnt lgkmcnt(7)
	v_mfma_f32_32x32x16_f16 v[34:49], v[204:207], v[108:111], v[130:145]
	v_exp_f32_e32 v5, v5
	v_mov_b32_e32 v83, 0
	v_exp_f32_e32 v6, v6
	v_add_f32_e32 v200, v200, v2
	v_exp_f32_e32 v7, v7
	v_add_f32_e32 v201, v201, v3
	s_waitcnt lgkmcnt(6)
	v_mfma_f32_32x32x16_f16 v[50:65], v[208:211], v[108:111], v[130:145]
	v_exp_f32_e32 v8, v8
	v_add_f32_e32 v202, v202, v4
	v_exp_f32_e32 v9, v9
	v_add_f32_e32 v83, v83, v5
	v_exp_f32_e32 v10, v10
	v_add_f32_e32 v200, v200, v6
	s_waitcnt lgkmcnt(5)
	v_mfma_f32_32x32x16_f16 v[34:49], v[212:215], v[104:107], v[34:49]
	v_exp_f32_e32 v11, v11
	v_add_f32_e32 v201, v201, v7
	v_exp_f32_e32 v12, v12
	v_add_f32_e32 v202, v202, v8
	v_exp_f32_e32 v13, v13
	v_add_f32_e32 v83, v83, v9
	s_waitcnt lgkmcnt(4)
	v_mfma_f32_32x32x16_f16 v[50:65], v[216:219], v[104:107], v[50:65]
	v_exp_f32_e32 v14, v14
	v_add_f32_e32 v200, v200, v10
	v_exp_f32_e32 v15, v15
	v_add_f32_e32 v201, v201, v11
	v_exp_f32_e32 v16, v16
	v_add_f32_e32 v202, v202, v12
	s_waitcnt lgkmcnt(3)
	v_mfma_f32_32x32x16_f16 v[34:49], v[220:223], v[100:103], v[34:49]
	v_exp_f32_e32 v17, v17
	v_add_f32_e32 v83, v83, v13
	v_exp_f32_e32 v18, v18
	v_add_f32_e32 v200, v200, v14
	v_exp_f32_e32 v19, v19
	v_add_f32_e32 v201, v201, v15
	s_waitcnt lgkmcnt(2)
	v_mfma_f32_32x32x16_f16 v[50:65], v[224:227], v[100:103], v[50:65]
	v_exp_f32_e32 v20, v20
	v_add_f32_e32 v202, v202, v16
	v_exp_f32_e32 v21, v21
	v_add_f32_e32 v83, v83, v17
	v_exp_f32_e32 v22, v22
	v_add_f32_e32 v200, v200, v18
	s_waitcnt lgkmcnt(1)
	v_mfma_f32_32x32x16_f16 v[34:49], v[228:231], v[96:99], v[34:49]
	v_exp_f32_e32 v23, v23
	v_add_f32_e32 v201, v201, v19
	v_exp_f32_e32 v24, v24
	v_add_f32_e32 v202, v202, v20
	v_exp_f32_e32 v25, v25
	v_add_f32_e32 v83, v83, v21
	s_waitcnt lgkmcnt(0)
	v_mfma_f32_32x32x16_f16 v[50:65], v[232:235], v[96:99], v[50:65]
	v_exp_f32_e32 v26, v26
	v_add_f32_e32 v200, v200, v22
	v_exp_f32_e32 v27, v27
	v_add_f32_e32 v201, v201, v23
	v_exp_f32_e32 v28, v28
	v_add_f32_e32 v202, v202, v24
	v_exp_f32_e32 v29, v29
	v_add_f32_e32 v83, v83, v25
	v_exp_f32_e32 v30, v30
	v_add_f32_e32 v200, v200, v26
	v_exp_f32_e32 v31, v31
	v_add_f32_e32 v201, v201, v27
	v_exp_f32_e32 v32, v32
	v_add_f32_e32 v202, v202, v28
	v_exp_f32_e32 v33, v33
	v_add_f32_e32 v83, v83, v29
	v_add_f32_e32 v200, v200, v30
	v_add_f32_e32 v201, v201, v31
	v_add_f32_e32 v202, v202, v32
	v_add_f32_e32 v83, v83, v33
	v_add_f32_e32 v200, v200, v201
	v_add_f32_e32 v202, v202, v83
	v_add_f32_e32 v200, v200, v202
	v_add_f32_e32 v82, v82, v200
	v_max3_f32 v84, v34, v35, v36
	v_max3_f32 v85, v50, v51, v52
	v_max3_f32 v84, v84, v37, v38
	v_max3_f32 v85, v85, v53, v54
	v_max3_f32 v84, v84, v39, v40
	v_max3_f32 v85, v85, v55, v56
	v_max3_f32 v84, v84, v41, v42
	v_max3_f32 v85, v85, v57, v58
	v_max3_f32 v84, v84, v43, v44
	v_max3_f32 v85, v85, v59, v60
	v_max3_f32 v84, v84, v45, v46
	v_max3_f32 v85, v85, v61, v62
	v_max3_f32 v84, v84, v47, v48
	v_max3_f32 v85, v85, v63, v64
	v_max3_f32 v84, v84, v49, v65
	s_nop 0
	v_max_f32_e32 v84, v84, v85
	s_nop 0
	v_cmp_lt_f32_e32 vcc, s11, v84
	s_cbranch_vccnz .Lp1_rare_d0b
.Lp1_back_d0b:
	s_waitcnt lgkmcnt(0)
	s_barrier
	s_waitcnt vmcnt(0)
	ds_write_b128 v77, v[112:115]
	ds_write_b128 v78, v[116:119]
	ds_write_b128 v77, v[120:123] offset:9216
	ds_write_b128 v78, v[124:127] offset:9216
	global_load_dwordx4 v[146:149], v128, s[24:25]
	global_load_dwordx4 v[150:153], v86, s[24:25]
	s_add_u32 s24, s24, 0x2000
	s_addc_u32 s25, s25, 0
	global_load_dwordx4 v[154:157], v128, s[24:25]
	global_load_dwordx4 v[158:161], v86, s[24:25]
	s_add_u32 s24, s24, 0x2000
	s_addc_u32 s25, s25, 0
	ds_read_b128 v[168:171], v87
	ds_read_b128 v[172:175], v87 offset:4608
	ds_read_b128 v[176:179], v87 offset:32
	ds_read_b128 v[180:183], v87 offset:4640
	ds_read_b128 v[184:187], v87 offset:64
	ds_read_b128 v[188:191], v87 offset:4672
	ds_read_b128 v[192:195], v87 offset:96
	ds_read_b128 v[196:199], v87 offset:4704
	v_exp_f32_e32 v34, v34
	v_mov_b32_e32 v200, 0
	v_exp_f32_e32 v35, v35
	v_mov_b32_e32 v201, 0
	v_exp_f32_e32 v36, v36
	v_mov_b32_e32 v202, 0
	s_waitcnt lgkmcnt(7)
	v_mfma_f32_32x32x16_f16 v[2:17], v[168:171], v[108:111], v[130:145]
	v_exp_f32_e32 v37, v37
	v_mov_b32_e32 v83, 0
	v_exp_f32_e32 v38, v38
	v_add_f32_e32 v200, v200, v34
	v_exp_f32_e32 v39, v39
	v_add_f32_e32 v201, v201, v35
	s_waitcnt lgkmcnt(6)
	v_mfma_f32_32x32x16_f16 v[18:33], v[172:175], v[108:111], v[130:145]
	v_exp_f32_e32 v40, v40
	v_add_f32_e32 v202, v202, v36
	v_exp_f32_e32 v41, v41
	v_add_f32_e32 v83, v83, v37
	v_exp_f32_e32 v42, v42
	v_add_f32_e32 v200, v200, v38
	s_waitcnt lgkmcnt(5)
	v_mfma_f32_32x32x16_f16 v[2:17], v[176:179], v[104:107], v[2:17]
	v_exp_f32_e32 v43, v43
	v_add_f32_e32 v201, v201, v39
	v_exp_f32_e32 v44, v44
	v_add_f32_e32 v202, v202, v40
	v_exp_f32_e32 v45, v45
	v_add_f32_e32 v83, v83, v41
	s_waitcnt lgkmcnt(4)
	v_mfma_f32_32x32x16_f16 v[18:33], v[180:183], v[104:107], v[18:33]
	v_exp_f32_e32 v46, v46
	v_add_f32_e32 v200, v200, v42
	v_exp_f32_e32 v47, v47
	v_add_f32_e32 v201, v201, v43
	v_exp_f32_e32 v48, v48
	v_add_f32_e32 v202, v202, v44
	s_waitcnt lgkmcnt(3)
	v_mfma_f32_32x32x16_f16 v[2:17], v[184:187], v[100:103], v[2:17]
	v_exp_f32_e32 v49, v49
	v_add_f32_e32 v83, v83, v45
	v_exp_f32_e32 v50, v50
	v_add_f32_e32 v200, v200, v46
	v_exp_f32_e32 v51, v51
	v_add_f32_e32 v201, v201, v47
	s_waitcnt lgkmcnt(2)
	v_mfma_f32_32x32x16_f16 v[18:33], v[188:191], v[100:103], v[18:33]
	v_exp_f32_e32 v52, v52
	v_add_f32_e32 v202, v202, v48
	v_exp_f32_e32 v53, v53
	v_add_f32_e32 v83, v83, v49
	v_exp_f32_e32 v54, v54
	v_add_f32_e32 v200, v200, v50
	s_waitcnt lgkmcnt(1)
	v_mfma_f32_32x32x16_f16 v[2:17], v[192:195], v[96:99], v[2:17]
	v_exp_f32_e32 v55, v55
	v_add_f32_e32 v201, v201, v51
	v_exp_f32_e32 v56, v56
	v_add_f32_e32 v202, v202, v52
	v_exp_f32_e32 v57, v57
	v_add_f32_e32 v83, v83, v53
	s_waitcnt lgkmcnt(0)
	v_mfma_f32_32x32x16_f16 v[18:33], v[196:199], v[96:99], v[18:33]
	ds_read_b128 v[204:207], v87 offset:9216
	ds_read_b128 v[208:211], v87 offset:13824
	ds_read_b128 v[212:215], v87 offset:9248
	ds_read_b128 v[216:219], v87 offset:13856
	ds_read_b128 v[220:223], v87 offset:9280
	ds_read_b128 v[224:227], v87 offset:13888
	ds_read_b128 v[228:231], v87 offset:9312
	ds_read_b128 v[232:235], v87 offset:13920
	v_exp_f32_e32 v58, v58
	v_add_f32_e32 v200, v200, v54
	v_exp_f32_e32 v59, v59
	v_add_f32_e32 v201, v201, v55
	v_exp_f32_e32 v60, v60
	v_add_f32_e32 v202, v202, v56
	v_exp_f32_e32 v61, v61
	v_add_f32_e32 v83, v83, v57
	v_exp_f32_e32 v62, v62
	v_add_f32_e32 v200, v200, v58
	v_exp_f32_e32 v63, v63
	v_add_f32_e32 v201, v201, v59
	v_exp_f32_e32 v64, v64
	v_add_f32_e32 v202, v202, v60
	v_exp_f32_e32 v65, v65
	v_add_f32_e32 v83, v83, v61
	v_add_f32_e32 v200, v200, v62
	v_add_f32_e32 v201, v201, v63
	v_add_f32_e32 v202, v202, v64
	v_add_f32_e32 v83, v83, v65
	v_add_f32_e32 v200, v200, v201
	v_add_f32_e32 v202, v202, v83
	v_add_f32_e32 v200, v200, v202
	v_add_f32_e32 v82, v82, v200
	v_max3_f32 v84, v2, v3, v4
	v_max3_f32 v85, v18, v19, v20
	v_max3_f32 v84, v84, v5, v6
	v_max3_f32 v85, v85, v21, v22
	v_max3_f32 v84, v84, v7, v8
	v_max3_f32 v85, v85, v23, v24
	v_max3_f32 v84, v84, v9, v10
	v_max3_f32 v85, v85, v25, v26
	v_max3_f32 v84, v84, v11, v12
	v_max3_f32 v85, v85, v27, v28
	v_max3_f32 v84, v84, v13, v14
	v_max3_f32 v85, v85, v29, v30
	v_max3_f32 v84, v84, v15, v16
	v_max3_f32 v85, v85, v31, v32
	v_max3_f32 v84, v84, v17, v33
	s_nop 0
	v_max_f32_e32 v84, v84, v85
	s_nop 0
	v_cmp_lt_f32_e32 vcc, s11, v84
	s_cbranch_vccnz .Lp1_rare_d1a
